# P1: first K-iteration of units 1 and 2 no longer waits for the previous unit's epilogue stores at phase 4 (store-tolerant vmcnt), their completion is required only at phase 6
# baseline (speedup 1.0000x reference)
.LBB2_40:
	s_andn2_b64 vcc, exec, s[18:19]
	s_cbranch_vccnz .LBB2_42
	s_add_u32 s76, s16, 0x4000
	s_addc_u32 s5, s75, 0
	s_and_b32 s77, s5, 0xffff
	s_mov_b32 s78, s6
	s_mov_b32 s79, s7
	s_mov_b32 m0, s42
	s_nop 0
	buffer_load_dwordx4 v196, s[76:79], 0 offen lds
	s_mov_b32 m0, s43
	s_nop 0
	buffer_load_dwordx4 v198, s[76:79], 0 offen lds
	s_cmp_lg_u32 s74, -2
	s_cbranch_scc1 .Lp1_w6
	s_cmp_eq_u32 s65, 1
	s_cbranch_scc1 .Lp1_w16
	s_cmp_eq_u32 s65, 2
	s_cbranch_scc1 .Lp1_w24
.Lp1_w6:
	s_waitcnt vmcnt(6)
	s_branch .LBB2_42
.Lp1_w16:
	s_waitcnt vmcnt(16)
	s_branch .LBB2_42
.Lp1_w24:
	s_waitcnt vmcnt(24)

.LBB2_44:
	s_waitcnt lgkmcnt(8)
	s_barrier
	s_waitcnt lgkmcnt(0)
	s_setprio 1
	v_mfma_i32_16x16x64_i8 v[124:127], v[128:131], v[184:187], v[124:127]
	v_mfma_i32_16x16x64_i8 v[120:123], v[132:135], v[184:187], v[120:123]
	v_mfma_i32_16x16x64_i8 v[108:111], v[128:131], v[172:175], v[108:111]
	v_mfma_i32_16x16x64_i8 v[104:107], v[132:135], v[172:175], v[104:107]
	v_mfma_i32_16x16x64_i8 v[96:99], v[128:131], v[168:171], v[96:99]
	v_mfma_i32_16x16x64_i8 v[88:91], v[132:135], v[168:171], v[88:91]
	v_mfma_i32_16x16x64_i8 v[80:83], v[128:131], v[160:163], v[80:83]
	v_mfma_i32_16x16x64_i8 v[72:75], v[132:135], v[160:163], v[72:75]
	v_mfma_i32_16x16x64_i8 v[124:127], v[140:143], v[188:191], v[124:127]
	v_mfma_i32_16x16x64_i8 v[120:123], v[136:139], v[188:191], v[120:123]
	v_mfma_i32_16x16x64_i8 v[108:111], v[140:143], v[176:179], v[108:111]
	v_mfma_i32_16x16x64_i8 v[104:107], v[136:139], v[176:179], v[104:107]
	v_mfma_i32_16x16x64_i8 v[96:99], v[140:143], v[180:183], v[96:99]
	v_mfma_i32_16x16x64_i8 v[88:91], v[136:139], v[180:183], v[88:91]
	v_mfma_i32_16x16x64_i8 v[80:83], v[140:143], v[164:167], v[80:83]
	v_mfma_i32_16x16x64_i8 v[72:75], v[136:139], v[164:167], v[72:75]
	s_setprio 0
	s_barrier
	s_add_i32 s5, 0, 0x1c000
	v_add_u32_e32 v148, s5, v199
	v_add_u32_e32 v152, s5, v200
	ds_read_b128 v[144:147], v148
	ds_read_b128 v[148:151], v148 offset:2048
	ds_read_b128 v[156:159], v152
	ds_read_b128 v[152:155], v152 offset:2048
	s_waitcnt vmcnt(8)
	s_and_b64 vcc, exec, s[0:1]
	s_cbranch_vccnz .LBB2_46
	s_add_u32 s76, s16, 0x80
	s_addc_u32 s5, s75, 0
	s_and_b32 s77, s5, 0xffff
	s_mov_b32 s78, s6
	s_mov_b32 s79, s7
	s_mov_b32 m0, s47
	s_nop 0
	buffer_load_dwordx4 v196, s[76:79], 0 offen lds
	s_mov_b32 m0, s48
	s_nop 0
	buffer_load_dwordx4 v198, s[76:79], 0 offen lds
